# top-k SLOT table stored transposed ([expert][row] instead of [row][expert]): per-list stores hit 32x fewer lines; combine phases read 16 lines per row
# speedup vs baseline: 1.0335x; 1.0335x over previous
; template <int VPT>
; __device__ __forceinline__ void topk_list(const Params& p, LAS unsigned char* lds, const float* a, int N, int cap, int rowbase, int mbase, int e) {
;     ...
;             const int i = tid * VPT + j, row = rowbase + i; int slot = -1;
;             if (k[j] > T) slot = gtb++;
;             else if (k[j] == T) { if (eqb < need) slot = G + eqb; ++eqb; }
;             if (slot >= 0) { const int m = mbase + slot; WSP(int, OFF_RIDX)[e * MEXP + m] = row; WSP(float, OFF_GATE)[e * MEXP + m] = __uint_as_float(k[j] >> 2); WSP(int, OFF_SLOT)[row * 16 + e] = m; }
;             else WSP(int, OFF_SLOT)[row * 16 + e] = -1;
.LBB0_738:
	s_or_b64 exec, exec, s[4:5]
	s_mul_i32 s98, s6, 0x4200
	v_add_u32_e32 v2, s98, v3
	v_ashrrev_i32_e32 v3, 31, v2
	v_lshl_add_u64 v[2:3], v[2:3], 2, s[80:81]
	global_store_dword v[2:3], v4, off

; template <int VPT>
; __device__ __forceinline__ void topk_list(const Params& p, LAS unsigned char* lds, const float* a, int N, int cap, int rowbase, int mbase, int e) {
;     ...
;     if (active) {
; #pragma unroll
;         for (int j = 0; j < VPT; ++j) {
;             const int i = tid * VPT + j, row = rowbase + i; int slot = -1;
;             if (k[j] > T) slot = gtb++;
;             else if (k[j] == T) { if (eqb < need) slot = G + eqb; ++eqb; }
;             if (slot >= 0) { const int m = mbase + slot; WSP(int, OFF_RIDX)[e * MEXP + m] = row; WSP(float, OFF_GATE)[e * MEXP + m] = __uint_as_float(k[j] >> 2); WSP(int, OFF_SLOT)[row * 16 + e] = m; }
;             else WSP(int, OFF_SLOT)[row * 16 + e] = -1;
;         }
.LBB0_840:
	s_or_b64 exec, exec, s[4:5]
	s_mul_i32 s98, s92, 0x4200
	v_add_u32_e32 v38, s98, v9
	v_ashrrev_i32_e32 v39, 31, v38
	v_lshl_add_u64 v[38:39], v[38:39], 2, s[80:81]
	global_store_dword v[38:39], v5, off
	s_and_saveexec_b64 s[4:5], s[70:71]
	s_xor_b64 s[4:5], exec, s[4:5]
	v_cmp_lt_i32_e64 s[24:25], v2, v11
	v_sub_u32_e32 v4, v2, v11
	v_add_u32_e32 v4, 0x400, v4
	v_cndmask_b32_e64 v5, 0, 1, s[64:65]
	s_and_b64 s[24:25], s[64:65], s[24:25]
	v_add_u32_e32 v2, v2, v5
	v_cndmask_b32_e64 v5, -1, v4, s[24:25]
	s_or_saveexec_b64 s[4:5], s[4:5]
	v_mov_b32_e32 v4, v3
	s_xor_b64 exec, exec, s[4:5]
	v_add_u32_e32 v4, 1, v3
	v_mov_b32_e32 v5, v3
	s_or_b64 exec, exec, s[4:5]
	v_add3_u32 v9, s68, v8, 1
	v_mov_b32_e32 v3, -1
	v_cmp_lt_i32_e64 s[24:25], -1, v5
	s_and_saveexec_b64 s[4:5], s[24:25]
	s_cbranch_execz .LBB0_846
	v_add_u32_e32 v3, s55, v5
	v_add_u32_e32 v38, s54, v3
	v_ashrrev_i32_e32 v39, 31, v38
	v_lshlrev_b64 v[38:39], 2, v[38:39]
	v_lshl_add_u64 v[40:41], s[84:85], 0, v[38:39]
	v_lshrrev_b32_e32 v5, 2, v36
	v_lshl_add_u64 v[36:37], s[2:3], 0, v[38:39]
	global_store_dword v[40:41], v9, off
	global_store_dword v[36:37], v5, off
.LBB0_846:
	s_or_b64 exec, exec, s[4:5]
	s_mul_i32 s98, s92, 0x4200
	v_add_u32_e32 v36, s98, v9
	v_ashrrev_i32_e32 v37, 31, v36
	v_lshl_add_u64 v[36:37], v[36:37], 2, s[80:81]
	global_store_dword v[36:37], v3, off
	s_and_saveexec_b64 s[4:5], s[66:67]
	s_xor_b64 s[4:5], exec, s[4:5]
	v_cmp_lt_i32_e64 s[24:25], v2, v11
	v_sub_u32_e32 v3, v2, v11
	v_add_u32_e32 v3, 0x400, v3
	v_cndmask_b32_e64 v5, 0, 1, s[60:61]
	s_and_b64 s[24:25], s[60:61], s[24:25]
	v_add_u32_e32 v2, v2, v5
	v_cndmask_b32_e64 v5, -1, v3, s[24:25]
	s_or_saveexec_b64 s[4:5], s[4:5]
	v_mov_b32_e32 v3, v4
	s_xor_b64 exec, exec, s[4:5]
	v_add_u32_e32 v3, 1, v4
	v_mov_b32_e32 v5, v4
	s_or_b64 exec, exec, s[4:5]
	v_add3_u32 v9, s68, v8, 2
	v_mov_b32_e32 v4, -1
	v_cmp_lt_i32_e64 s[24:25], -1, v5
	s_and_saveexec_b64 s[4:5], s[24:25]
	s_cbranch_execz .LBB0_852
	v_add_u32_e32 v4, s55, v5
	v_add_u32_e32 v36, s54, v4
	v_ashrrev_i32_e32 v37, 31, v36
	v_lshlrev_b64 v[36:37], 2, v[36:37]
	v_lshl_add_u64 v[38:39], s[84:85], 0, v[36:37]
	v_lshrrev_b32_e32 v5, 2, v35
	v_lshl_add_u64 v[36:37], s[2:3], 0, v[36:37]
	global_store_dword v[38:39], v9, off
	global_store_dword v[36:37], v5, off
.LBB0_852:
	s_or_b64 exec, exec, s[4:5]
	s_mul_i32 s98, s92, 0x4200
	v_add_u32_e32 v36, s98, v9
	v_ashrrev_i32_e32 v37, 31, v36
	v_lshl_add_u64 v[36:37], v[36:37], 2, s[80:81]
	global_store_dword v[36:37], v4, off
	s_and_saveexec_b64 s[4:5], s[62:63]
	s_xor_b64 s[4:5], exec, s[4:5]
	v_cmp_lt_i32_e64 s[24:25], v2, v11
	v_sub_u32_e32 v4, v2, v11
	v_add_u32_e32 v4, 0x400, v4
	v_cndmask_b32_e64 v5, 0, 1, s[56:57]
	s_and_b64 s[24:25], s[56:57], s[24:25]
	v_add_u32_e32 v2, v2, v5
	v_cndmask_b32_e64 v5, -1, v4, s[24:25]
	s_or_saveexec_b64 s[4:5], s[4:5]
	v_mov_b32_e32 v4, v3
	s_xor_b64 exec, exec, s[4:5]
	v_add_u32_e32 v4, 1, v3
	v_mov_b32_e32 v5, v3
	s_or_b64 exec, exec, s[4:5]
	v_add3_u32 v9, s68, v8, 3
	v_mov_b32_e32 v3, -1
	v_cmp_lt_i32_e64 s[24:25], -1, v5
	s_and_saveexec_b64 s[4:5], s[24:25]
	s_cbranch_execz .LBB0_858
	v_add_u32_e32 v3, s55, v5
	v_add_u32_e32 v36, s54, v3
	v_ashrrev_i32_e32 v37, 31, v36
	v_lshlrev_b64 v[36:37], 2, v[36:37]
	v_lshl_add_u64 v[38:39], s[84:85], 0, v[36:37]
	v_lshrrev_b32_e32 v5, 2, v34
	v_lshl_add_u64 v[34:35], s[2:3], 0, v[36:37]
	global_store_dword v[38:39], v9, off
	global_store_dword v[34:35], v5, off
.LBB0_858:
	s_or_b64 exec, exec, s[4:5]
	s_mul_i32 s98, s92, 0x4200
	v_add_u32_e32 v34, s98, v9
	v_ashrrev_i32_e32 v35, 31, v34
	v_lshl_add_u64 v[34:35], v[34:35], 2, s[80:81]
	global_store_dword v[34:35], v3, off
	s_and_saveexec_b64 s[4:5], s[58:59]
	s_xor_b64 s[4:5], exec, s[4:5]
	v_cmp_lt_i32_e64 s[24:25], v2, v11
	v_sub_u32_e32 v3, v2, v11
	v_add_u32_e32 v3, 0x400, v3
	v_cndmask_b32_e64 v5, 0, 1, s[48:49]
	s_and_b64 s[24:25], s[48:49], s[24:25]
	v_add_u32_e32 v2, v2, v5
	v_cndmask_b32_e64 v5, -1, v3, s[24:25]
	s_or_saveexec_b64 s[4:5], s[4:5]
	v_mov_b32_e32 v3, v4
	s_xor_b64 exec, exec, s[4:5]
	v_add_u32_e32 v3, 1, v4
	v_mov_b32_e32 v5, v4
	s_or_b64 exec, exec, s[4:5]
	v_add3_u32 v9, s68, v8, 4
	v_mov_b32_e32 v4, -1
	v_cmp_lt_i32_e64 s[24:25], -1, v5
	s_and_saveexec_b64 s[4:5], s[24:25]
	s_cbranch_execz .LBB0_864
	v_add_u32_e32 v4, s55, v5
	v_add_u32_e32 v34, s54, v4
	v_ashrrev_i32_e32 v35, 31, v34
	v_lshlrev_b64 v[34:35], 2, v[34:35]
	v_lshl_add_u64 v[36:37], s[84:85], 0, v[34:35]
	v_lshrrev_b32_e32 v5, 2, v33
	v_lshl_add_u64 v[34:35], s[2:3], 0, v[34:35]
	global_store_dword v[36:37], v9, off
	global_store_dword v[34:35], v5, off
.LBB0_864:
	s_or_b64 exec, exec, s[4:5]
	s_mul_i32 s98, s92, 0x4200
	v_add_u32_e32 v34, s98, v9
	v_ashrrev_i32_e32 v35, 31, v34
	v_lshl_add_u64 v[34:35], v[34:35], 2, s[80:81]
	global_store_dword v[34:35], v4, off
	s_and_saveexec_b64 s[4:5], s[50:51]
	s_xor_b64 s[4:5], exec, s[4:5]
	v_cmp_lt_i32_e64 s[24:25], v2, v11
	v_sub_u32_e32 v4, v2, v11
	v_add_u32_e32 v4, 0x400, v4
	v_cndmask_b32_e64 v5, 0, 1, s[44:45]
	s_and_b64 s[24:25], s[44:45], s[24:25]
	v_add_u32_e32 v2, v2, v5
	v_cndmask_b32_e64 v5, -1, v4, s[24:25]
	s_or_saveexec_b64 s[4:5], s[4:5]
	v_mov_b32_e32 v4, v3
	s_xor_b64 exec, exec, s[4:5]
	v_add_u32_e32 v4, 1, v3
	v_mov_b32_e32 v5, v3
	s_or_b64 exec, exec, s[4:5]
	v_add3_u32 v9, s68, v8, 5
	v_mov_b32_e32 v3, -1
	v_cmp_lt_i32_e64 s[24:25], -1, v5
	s_and_saveexec_b64 s[4:5], s[24:25]
	s_cbranch_execz .LBB0_870
	v_add_u32_e32 v3, s55, v5
	v_add_u32_e32 v34, s54, v3
	v_ashrrev_i32_e32 v35, 31, v34
	v_lshlrev_b64 v[34:35], 2, v[34:35]
	v_lshl_add_u64 v[36:37], s[84:85], 0, v[34:35]
	v_lshrrev_b32_e32 v5, 2, v32
	v_lshl_add_u64 v[32:33], s[2:3], 0, v[34:35]
	global_store_dword v[36:37], v9, off
	global_store_dword v[32:33], v5, off
; template <int VPT>
; __device__ __forceinline__ void topk_list(const Params& p, LAS unsigned char* lds, const float* a, int N, int cap, int rowbase, int mbase, int e) {
;     ...
;     if (active) {
; #pragma unroll
;         for (int j = 0; j < VPT; ++j) {
;             const int i = tid * VPT + j, row = rowbase + i; int slot = -1;
;             if (k[j] > T) slot = gtb++;
;             else if (k[j] == T) { if (eqb < need) slot = G + eqb; ++eqb; }
;             if (slot >= 0) { const int m = mbase + slot; WSP(int, OFF_RIDX)[e * MEXP + m] = row; WSP(float, OFF_GATE)[e * MEXP + m] = __uint_as_float(k[j] >> 2); WSP(int, OFF_SLOT)[row * 16 + e] = m; }
;             else WSP(int, OFF_SLOT)[row * 16 + e] = -1;
;         }
.LBB0_870:
	s_or_b64 exec, exec, s[4:5]
	s_mul_i32 s98, s92, 0x4200
	v_add_u32_e32 v32, s98, v9
	v_ashrrev_i32_e32 v33, 31, v32
	v_lshl_add_u64 v[32:33], v[32:33], 2, s[80:81]
	global_store_dword v[32:33], v3, off
	s_and_saveexec_b64 s[4:5], s[46:47]
	s_xor_b64 s[4:5], exec, s[4:5]
	v_cmp_lt_i32_e64 s[24:25], v2, v11
	v_sub_u32_e32 v3, v2, v11
	v_add_u32_e32 v3, 0x400, v3
	v_cndmask_b32_e64 v5, 0, 1, s[40:41]
	s_and_b64 s[24:25], s[40:41], s[24:25]
	v_add_u32_e32 v2, v2, v5
	v_cndmask_b32_e64 v5, -1, v3, s[24:25]
	s_or_saveexec_b64 s[4:5], s[4:5]
	v_mov_b32_e32 v3, v4
	s_xor_b64 exec, exec, s[4:5]
	v_add_u32_e32 v3, 1, v4
	v_mov_b32_e32 v5, v4
	s_or_b64 exec, exec, s[4:5]
	v_add3_u32 v9, s68, v8, 6
	v_mov_b32_e32 v4, -1
	v_cmp_lt_i32_e64 s[24:25], -1, v5
	s_and_saveexec_b64 s[4:5], s[24:25]
	s_cbranch_execz .LBB0_876
	v_add_u32_e32 v4, s55, v5
	v_add_u32_e32 v32, s54, v4
	v_ashrrev_i32_e32 v33, 31, v32
	v_lshlrev_b64 v[32:33], 2, v[32:33]
	v_lshl_add_u64 v[34:35], s[84:85], 0, v[32:33]
	v_lshrrev_b32_e32 v5, 2, v31
	v_lshl_add_u64 v[32:33], s[2:3], 0, v[32:33]
	global_store_dword v[34:35], v9, off
	global_store_dword v[32:33], v5, off
.LBB0_876:
	s_or_b64 exec, exec, s[4:5]
	s_mul_i32 s98, s92, 0x4200
	v_add_u32_e32 v32, s98, v9
	v_ashrrev_i32_e32 v33, 31, v32
	v_lshl_add_u64 v[32:33], v[32:33], 2, s[80:81]
	global_store_dword v[32:33], v4, off
	s_and_saveexec_b64 s[4:5], s[42:43]
	s_xor_b64 s[4:5], exec, s[4:5]
	v_cmp_lt_i32_e64 s[24:25], v2, v11
	v_sub_u32_e32 v4, v2, v11
	v_add_u32_e32 v4, 0x400, v4
	v_cndmask_b32_e64 v5, 0, 1, s[36:37]
	s_and_b64 s[24:25], s[36:37], s[24:25]
	v_add_u32_e32 v2, v2, v5
	v_cndmask_b32_e64 v5, -1, v4, s[24:25]
	s_or_saveexec_b64 s[4:5], s[4:5]
	v_mov_b32_e32 v4, v3
	s_xor_b64 exec, exec, s[4:5]
	v_add_u32_e32 v4, 1, v3
	v_mov_b32_e32 v5, v3
	s_or_b64 exec, exec, s[4:5]
	v_add3_u32 v9, s68, v8, 7
	v_mov_b32_e32 v3, -1
	v_cmp_lt_i32_e64 s[24:25], -1, v5
	s_and_saveexec_b64 s[4:5], s[24:25]
	s_cbranch_execz .LBB0_882
	v_add_u32_e32 v3, s55, v5
	v_add_u32_e32 v32, s54, v3
	v_ashrrev_i32_e32 v33, 31, v32
	v_lshlrev_b64 v[32:33], 2, v[32:33]
	v_lshl_add_u64 v[34:35], s[84:85], 0, v[32:33]
	v_lshrrev_b32_e32 v5, 2, v30
	v_lshl_add_u64 v[30:31], s[2:3], 0, v[32:33]
	global_store_dword v[34:35], v9, off
	global_store_dword v[30:31], v5, off
.LBB0_882:
	s_or_b64 exec, exec, s[4:5]
	s_mul_i32 s98, s92, 0x4200
	v_add_u32_e32 v30, s98, v9
	v_ashrrev_i32_e32 v31, 31, v30
	v_lshl_add_u64 v[30:31], v[30:31], 2, s[80:81]
	global_store_dword v[30:31], v3, off
	s_and_saveexec_b64 s[4:5], s[38:39]
	s_xor_b64 s[4:5], exec, s[4:5]
	v_cmp_lt_i32_e64 s[24:25], v2, v11
	v_sub_u32_e32 v3, v2, v11
	v_add_u32_e32 v3, 0x400, v3
	v_cndmask_b32_e64 v5, 0, 1, s[30:31]
	s_and_b64 s[24:25], s[30:31], s[24:25]
	v_add_u32_e32 v2, v2, v5
	v_cndmask_b32_e64 v5, -1, v3, s[24:25]
	s_or_saveexec_b64 s[4:5], s[4:5]
	v_mov_b32_e32 v3, v4
	s_xor_b64 exec, exec, s[4:5]
	v_add_u32_e32 v3, 1, v4
	v_mov_b32_e32 v5, v4
	s_or_b64 exec, exec, s[4:5]
	v_add3_u32 v9, s68, v8, 8
	v_mov_b32_e32 v4, -1
	v_cmp_lt_i32_e64 s[24:25], -1, v5
	s_and_saveexec_b64 s[4:5], s[24:25]
	s_cbranch_execz .LBB0_888
	v_add_u32_e32 v4, s55, v5
	v_add_u32_e32 v30, s54, v4
	v_ashrrev_i32_e32 v31, 31, v30
	v_lshlrev_b64 v[30:31], 2, v[30:31]
	v_lshl_add_u64 v[32:33], s[84:85], 0, v[30:31]
	v_lshrrev_b32_e32 v5, 2, v29
	v_lshl_add_u64 v[30:31], s[2:3], 0, v[30:31]
	global_store_dword v[32:33], v9, off
	global_store_dword v[30:31], v5, off
.LBB0_888:
	s_or_b64 exec, exec, s[4:5]
	s_mul_i32 s98, s92, 0x4200
	v_add_u32_e32 v30, s98, v9
	v_ashrrev_i32_e32 v31, 31, v30
	v_lshl_add_u64 v[30:31], v[30:31], 2, s[80:81]
	global_store_dword v[30:31], v4, off
	s_and_saveexec_b64 s[4:5], s[34:35]
	s_xor_b64 s[4:5], exec, s[4:5]
	v_cmp_lt_i32_e64 s[24:25], v2, v11
	v_sub_u32_e32 v4, v2, v11
	v_add_u32_e32 v4, 0x400, v4
	v_cndmask_b32_e64 v5, 0, 1, s[26:27]
	s_and_b64 s[24:25], s[26:27], s[24:25]
	v_add_u32_e32 v2, v2, v5
	v_cndmask_b32_e64 v5, -1, v4, s[24:25]
	s_or_saveexec_b64 s[4:5], s[4:5]
	v_mov_b32_e32 v4, v3
	s_xor_b64 exec, exec, s[4:5]
	v_add_u32_e32 v4, 1, v3
	v_mov_b32_e32 v5, v3
	s_or_b64 exec, exec, s[4:5]
	v_add3_u32 v9, s68, v8, 9
	v_mov_b32_e32 v3, -1
	v_cmp_lt_i32_e64 s[24:25], -1, v5
	s_and_saveexec_b64 s[4:5], s[24:25]
	s_cbranch_execz .LBB0_894
	v_add_u32_e32 v3, s55, v5
	v_add_u32_e32 v30, s54, v3
	v_ashrrev_i32_e32 v31, 31, v30
	v_lshlrev_b64 v[30:31], 2, v[30:31]
	v_lshl_add_u64 v[32:33], s[84:85], 0, v[30:31]
	v_lshrrev_b32_e32 v5, 2, v28
	v_lshl_add_u64 v[28:29], s[2:3], 0, v[30:31]
	global_store_dword v[32:33], v9, off
	global_store_dword v[28:29], v5, off
.LBB0_894:
	s_or_b64 exec, exec, s[4:5]
	s_mul_i32 s98, s92, 0x4200
	v_add_u32_e32 v28, s98, v9
	v_ashrrev_i32_e32 v29, 31, v28
	v_lshl_add_u64 v[28:29], v[28:29], 2, s[80:81]
	global_store_dword v[28:29], v3, off
	s_and_saveexec_b64 s[4:5], s[28:29]
	s_xor_b64 s[4:5], exec, s[4:5]
	v_cmp_lt_i32_e64 s[24:25], v2, v11
	v_sub_u32_e32 v3, v2, v11
	v_add_u32_e32 v3, 0x400, v3
	v_cndmask_b32_e64 v5, 0, 1, s[20:21]
	s_and_b64 s[20:21], s[20:21], s[24:25]
	v_add_u32_e32 v2, v2, v5
	v_cndmask_b32_e64 v5, -1, v3, s[20:21]
	s_or_saveexec_b64 s[4:5], s[4:5]
	v_mov_b32_e32 v3, v4
	s_xor_b64 exec, exec, s[4:5]
	v_add_u32_e32 v3, 1, v4
	v_mov_b32_e32 v5, v4
	s_or_b64 exec, exec, s[4:5]
	v_add3_u32 v9, s68, v8, 10
	v_mov_b32_e32 v4, -1
	v_cmp_lt_i32_e64 s[20:21], -1, v5
	s_and_saveexec_b64 s[4:5], s[20:21]
	s_cbranch_execz .LBB0_900
	v_add_u32_e32 v4, s55, v5
	v_add_u32_e32 v28, s54, v4
	v_ashrrev_i32_e32 v29, 31, v28
	v_lshlrev_b64 v[28:29], 2, v[28:29]
	v_lshl_add_u64 v[30:31], s[84:85], 0, v[28:29]
	v_lshrrev_b32_e32 v5, 2, v27
	v_lshl_add_u64 v[28:29], s[2:3], 0, v[28:29]
	global_store_dword v[30:31], v9, off
	global_store_dword v[28:29], v5, off
; template <int VPT>
; __device__ __forceinline__ void topk_list(const Params& p, LAS unsigned char* lds, const float* a, int N, int cap, int rowbase, int mbase, int e) {
;     ...
;     if (active) {
; #pragma unroll
;         for (int j = 0; j < VPT; ++j) {
;             const int i = tid * VPT + j, row = rowbase + i; int slot = -1;
;             if (k[j] > T) slot = gtb++;
;             else if (k[j] == T) { if (eqb < need) slot = G + eqb; ++eqb; }
;             if (slot >= 0) { const int m = mbase + slot; WSP(int, OFF_RIDX)[e * MEXP + m] = row; WSP(float, OFF_GATE)[e * MEXP + m] = __uint_as_float(k[j] >> 2); WSP(int, OFF_SLOT)[row * 16 + e] = m; }
;             else WSP(int, OFF_SLOT)[row * 16 + e] = -1;
;         }
.LBB0_900:
	s_or_b64 exec, exec, s[4:5]
	s_mul_i32 s98, s92, 0x4200
	v_add_u32_e32 v28, s98, v9
	v_ashrrev_i32_e32 v29, 31, v28
	v_lshl_add_u64 v[28:29], v[28:29], 2, s[80:81]
	global_store_dword v[28:29], v4, off
	s_and_saveexec_b64 s[4:5], s[22:23]
	s_xor_b64 s[4:5], exec, s[4:5]
	v_cmp_lt_i32_e64 s[20:21], v2, v11
	v_sub_u32_e32 v4, v2, v11
	v_add_u32_e32 v4, 0x400, v4
	v_cndmask_b32_e64 v5, 0, 1, s[16:17]
	s_and_b64 s[16:17], s[16:17], s[20:21]
	v_add_u32_e32 v2, v2, v5
	v_cndmask_b32_e64 v5, -1, v4, s[16:17]
	s_or_saveexec_b64 s[4:5], s[4:5]
	v_mov_b32_e32 v4, v3
	s_xor_b64 exec, exec, s[4:5]
	v_add_u32_e32 v4, 1, v3
	v_mov_b32_e32 v5, v3
	s_or_b64 exec, exec, s[4:5]
	v_add3_u32 v9, s68, v8, 11
	v_mov_b32_e32 v3, -1
	v_cmp_lt_i32_e64 s[16:17], -1, v5
	s_and_saveexec_b64 s[4:5], s[16:17]
	s_cbranch_execz .LBB0_906
	v_add_u32_e32 v3, s55, v5
	v_add_u32_e32 v28, s54, v3
	v_ashrrev_i32_e32 v29, 31, v28
	v_lshlrev_b64 v[28:29], 2, v[28:29]
	v_lshl_add_u64 v[30:31], s[84:85], 0, v[28:29]
	v_lshrrev_b32_e32 v5, 2, v26
	v_lshl_add_u64 v[26:27], s[2:3], 0, v[28:29]
	global_store_dword v[30:31], v9, off
	global_store_dword v[26:27], v5, off
.LBB0_906:
	s_or_b64 exec, exec, s[4:5]
	s_mul_i32 s98, s92, 0x4200
	v_add_u32_e32 v26, s98, v9
	v_ashrrev_i32_e32 v27, 31, v26
	v_lshl_add_u64 v[26:27], v[26:27], 2, s[80:81]
	global_store_dword v[26:27], v3, off
	s_and_saveexec_b64 s[4:5], s[18:19]
	s_xor_b64 s[4:5], exec, s[4:5]
	v_cmp_lt_i32_e64 s[16:17], v2, v11
	v_sub_u32_e32 v3, v2, v11
	v_add_u32_e32 v3, 0x400, v3
	v_cndmask_b32_e64 v5, 0, 1, s[12:13]
	s_and_b64 s[12:13], s[12:13], s[16:17]
	v_add_u32_e32 v2, v2, v5
	v_cndmask_b32_e64 v5, -1, v3, s[12:13]
	s_or_saveexec_b64 s[4:5], s[4:5]
	v_mov_b32_e32 v3, v4
	s_xor_b64 exec, exec, s[4:5]
	v_add_u32_e32 v3, 1, v4
	v_mov_b32_e32 v5, v4
	s_or_b64 exec, exec, s[4:5]
	v_add3_u32 v9, s68, v8, 12
	v_mov_b32_e32 v4, -1
	v_cmp_lt_i32_e64 s[12:13], -1, v5
	s_and_saveexec_b64 s[4:5], s[12:13]
	s_cbranch_execz .LBB0_912
	v_add_u32_e32 v4, s55, v5
	v_add_u32_e32 v26, s54, v4
	v_ashrrev_i32_e32 v27, 31, v26
	v_lshlrev_b64 v[26:27], 2, v[26:27]
	v_lshl_add_u64 v[28:29], s[84:85], 0, v[26:27]
	v_lshrrev_b32_e32 v5, 2, v25
	v_lshl_add_u64 v[26:27], s[2:3], 0, v[26:27]
	global_store_dword v[28:29], v9, off
	global_store_dword v[26:27], v5, off
.LBB0_912:
	s_or_b64 exec, exec, s[4:5]
	s_mul_i32 s98, s92, 0x4200
	v_add_u32_e32 v26, s98, v9
	v_ashrrev_i32_e32 v27, 31, v26
	v_lshl_add_u64 v[26:27], v[26:27], 2, s[80:81]
	global_store_dword v[26:27], v4, off
	s_and_saveexec_b64 s[4:5], s[14:15]
	s_xor_b64 s[4:5], exec, s[4:5]
	v_cmp_lt_i32_e64 s[12:13], v2, v11
	v_sub_u32_e32 v4, v2, v11
	v_add_u32_e32 v4, 0x400, v4
	v_cndmask_b32_e64 v5, 0, 1, s[8:9]
	s_and_b64 s[8:9], s[8:9], s[12:13]
	v_add_u32_e32 v2, v2, v5
	v_cndmask_b32_e64 v5, -1, v4, s[8:9]
	s_or_saveexec_b64 s[4:5], s[4:5]
	v_mov_b32_e32 v4, v3
	s_xor_b64 exec, exec, s[4:5]
	v_add_u32_e32 v4, 1, v3
	v_mov_b32_e32 v5, v3
	s_or_b64 exec, exec, s[4:5]
	v_add3_u32 v9, s68, v8, 13
	v_mov_b32_e32 v3, -1
	v_cmp_lt_i32_e64 s[8:9], -1, v5
	s_and_saveexec_b64 s[4:5], s[8:9]
	s_cbranch_execz .LBB0_918
	v_add_u32_e32 v3, s55, v5
	v_add_u32_e32 v26, s54, v3
	v_ashrrev_i32_e32 v27, 31, v26
	v_lshlrev_b64 v[26:27], 2, v[26:27]
	v_lshl_add_u64 v[28:29], s[84:85], 0, v[26:27]
	v_lshrrev_b32_e32 v5, 2, v24
	v_lshl_add_u64 v[24:25], s[2:3], 0, v[26:27]
	global_store_dword v[28:29], v9, off
	global_store_dword v[24:25], v5, off
.LBB0_918:
	s_or_b64 exec, exec, s[4:5]
	s_mul_i32 s98, s92, 0x4200
	v_add_u32_e32 v24, s98, v9
	v_ashrrev_i32_e32 v25, 31, v24
	v_lshl_add_u64 v[24:25], v[24:25], 2, s[80:81]
	global_store_dword v[24:25], v3, off
	s_and_saveexec_b64 s[4:5], s[10:11]
	s_xor_b64 s[4:5], exec, s[4:5]
	v_cmp_lt_i32_e64 s[8:9], v2, v11
	v_sub_u32_e32 v3, v2, v11
	v_add_u32_e32 v3, 0x400, v3
	v_cndmask_b32_e64 v5, 0, 1, s[6:7]
	s_and_b64 s[6:7], s[6:7], s[8:9]
	v_add_u32_e32 v2, v2, v5
	v_cndmask_b32_e64 v9, -1, v3, s[6:7]
	s_or_saveexec_b64 s[4:5], s[4:5]
	v_mov_b32_e32 v5, v4
	s_xor_b64 exec, exec, s[4:5]
	v_add_u32_e32 v5, 1, v4
	v_mov_b32_e32 v9, v4
	s_or_b64 exec, exec, s[4:5]
	v_add3_u32 v10, s68, v8, 14
	v_mov_b32_e32 v3, -1
	v_cmp_lt_i32_e64 s[6:7], -1, v9
	v_mov_b32_e32 v4, -1
	s_and_saveexec_b64 s[4:5], s[6:7]
	s_cbranch_execz .LBB0_924
	v_add_u32_e32 v4, s55, v9
	v_add_u32_e32 v24, s54, v4
	v_ashrrev_i32_e32 v25, 31, v24
	v_lshlrev_b64 v[24:25], 2, v[24:25]
	v_lshl_add_u64 v[26:27], s[84:85], 0, v[24:25]
	v_lshrrev_b32_e32 v9, 2, v23
	v_lshl_add_u64 v[24:25], s[2:3], 0, v[24:25]
	global_store_dword v[26:27], v10, off
	global_store_dword v[24:25], v9, off
.LBB0_924:
	s_or_b64 exec, exec, s[4:5]
	v_cmp_lt_i32_e64 s[6:7], v2, v11
	v_sub_u32_e32 v2, v2, v11
	s_mul_i32 s98, s92, 0x4200
	v_add_u32_e32 v24, s98, v10
	v_add_u32_e32 v2, 0x400, v2
	s_and_b64 s[0:1], s[0:1], s[6:7]
	v_ashrrev_i32_e32 v25, 31, v24
	v_cndmask_b32_e64 v2, -1, v2, s[0:1]
	v_lshl_add_u64 v[24:25], v[24:25], 2, s[80:81]
	v_cndmask_b32_e32 v2, v2, v5, vcc
	global_store_dword v[24:25], v4, off
	v_add3_u32 v4, s68, v8, 15
	v_cmp_lt_i32_e32 vcc, -1, v2
	s_and_saveexec_b64 s[0:1], vcc
	s_cbranch_execz .LBB0_926
	v_add_u32_e32 v3, s55, v2
	v_add_u32_e32 v8, s54, v3
	v_ashrrev_i32_e32 v9, 31, v8
	v_lshlrev_b64 v[8:9], 2, v[8:9]
	v_lshl_add_u64 v[10:11], s[84:85], 0, v[8:9]
	v_lshrrev_b32_e32 v2, 2, v6
	v_lshl_add_u64 v[8:9], s[2:3], 0, v[8:9]
	global_store_dword v[10:11], v4, off
	global_store_dword v[8:9], v2, off
.LBB0_926:
	s_or_b64 exec, exec, s[0:1]
	s_mul_i32 s98, s92, 0x4200
	v_add_u32_e32 v4, s98, v4
	v_ashrrev_i32_e32 v5, 31, v4
	v_lshl_add_u64 v[4:5], v[4:5], 2, s[80:81]
	global_store_dword v[4:5], v3, off

; template <bool LAST>
; __device__ __forceinline__ void ph_combine(const int vc, const Params& p, int layer, int rows) {
;     ...
;     u32x2 xn[4]; int son = -1;
;     auto prefetch = [&](int row) { const bf16_t* xr = WSP(bf16_t, OFF_X) + (size_t)row * D;
; #pragma unroll
;         for (int j = 0; j < 4; ++j) xn[j] = ((const u32x2*)xr)[lane + 64 * j];
;         son = WSP(int, OFF_SLOT)[row * 16 + (lane & 15)]; };
;     if (gw < rows) prefetch(gw);
;     for (int row = gw; row < rows; row += NGW) {
;         f32x4 v[4], acc[4];
; #pragma unroll
;         for (int j = 0; j < 4; ++j) { v[j] = (f32x4){__uint_as_float(xn[j].x << 16), __uint_as_float(xn[j].x & 0xffff0000u), __uint_as_float(xn[j].y << 16), __uint_as_float(xn[j].y & 0xffff0000u)}; acc[j] = (f32x4){0.f, 0.f, 0.f, 0.f}; }
;         const int so = son;
;         prefetch(row + NGW < rows ? row + NGW : row);
.LBB0_1173:
	s_or_b64 exec, exec, s[0:1]
	s_waitcnt lgkmcnt(0)
	v_mov_b32_e32 v1, v0
	s_barrier
	s_add_u32 s4, s90, 0x51a25600
	v_ashrrev_i32_e32 v2, 6, v1
	v_add_u32_e32 v28, v2, v198
	s_movk_i32 s20, 0x4200
	s_addc_u32 s5, s91, 0
	v_cmp_gt_i32_e32 vcc, s20, v28
	s_and_saveexec_b64 s[2:3], vcc
	s_cbranch_execz .LBB0_1194
	s_add_u32 s0, s90, 0x13600
	v_ashrrev_i32_e32 v29, 31, v28
	v_and_b32_e32 v2, 63, v1
	s_addc_u32 s1, s91, 0
	v_lshlrev_b64 v[4:5], 11, v[28:29]
	v_lshl_add_u64 v[6:7], s[0:1], 0, v[4:5]
	v_mov_b32_e32 v5, 0
	v_lshlrev_b32_e32 v4, 3, v2
	v_lshl_add_u64 v[6:7], v[6:7], 0, v[4:5]
	v_and_b32_e32 v1, 15, v1
	global_load_dwordx2 v[44:45], v[6:7], off
	global_load_dwordx2 v[42:43], v[6:7], off offset:512
	global_load_dwordx2 v[40:41], v[6:7], off offset:1024
	global_load_dwordx2 v[38:39], v[6:7], off offset:1536
	s_add_u32 s6, s90, 0x51b87600
	v_mul_u32_u24_e32 v6, 0x4200, v1
	v_add_u32_e32 v6, v6, v28
	s_addc_u32 s7, s91, 0
	v_ashrrev_i32_e32 v7, 31, v6
	v_lshl_add_u64 v[6:7], v[6:7], 2, s[6:7]
	global_load_dword v23, v[6:7], off
	v_or_b32_e32 v22, 64, v2
	v_or_b32_e32 v24, 0x80, v2
	v_or_b32_e32 v26, 0xc0, v2
	v_lshl_add_u64 v[6:7], s[0:1], 0, v[4:5]
	s_add_u32 s0, s24, 0x1000
	s_addc_u32 s1, s25, 0
	v_lshlrev_b32_e32 v8, 4, v2
	v_mov_b32_e32 v9, v5
	v_lshlrev_b32_e32 v10, 4, v22
	v_mov_b32_e32 v11, v5
	v_lshlrev_b32_e32 v12, 4, v24
	v_mov_b32_e32 v13, v5
	v_lshlrev_b32_e32 v14, 4, v26
	v_mov_b32_e32 v15, v5
	s_mov_b64 s[8:9], 0x1000
	v_lshl_add_u64 v[8:9], s[0:1], 0, v[8:9]
	v_lshl_add_u64 v[10:11], s[0:1], 0, v[10:11]
	v_lshl_add_u64 v[12:13], s[0:1], 0, v[12:13]
	v_lshl_add_u64 v[14:15], s[0:1], 0, v[14:15]
	v_lshl_add_u64 v[16:17], s[84:85], 0, v[4:5]
	v_lshl_add_u64 v[18:19], s[82:83], 0, v[4:5]
	v_lshl_add_u64 v[20:21], s[90:91], 0, v[4:5]
	s_mov_b64 s[10:11], 0
	s_movk_i32 s21, 0x41ff
	s_movk_i32 s22, 0x4000
	s_mov_b32 s13, 0
	s_mov_b32 s23, 0x1ab13000
	s_mov_b64 s[14:15], 0x51a18600
	v_lshlrev_b32_e32 v22, 4, v22
	v_lshlrev_b32_e32 v24, 4, v24
	v_lshlrev_b32_e32 v26, 4, v26
	v_mov_b32_e32 v3, 0x358637bd
	s_mov_b32 s24, 0x800000
	s_branch .LBB0_1176

; template <bool LAST>
; __device__ __forceinline__ void ph_combine(const int vc, const Params& p, int layer, int rows) {
;     ...
;     for (int row = gw; row < rows; row += NGW) {
;         f32x4 v[4], acc[4];
; #pragma unroll
;         for (int j = 0; j < 4; ++j) { v[j] = (f32x4){__uint_as_float(xn[j].x << 16), __uint_as_float(xn[j].x & 0xffff0000u), __uint_as_float(xn[j].y << 16), __uint_as_float(xn[j].y & 0xffff0000u)}; acc[j] = (f32x4){0.f, 0.f, 0.f, 0.f}; }
;         const int so = son;
;         prefetch(row + NGW < rows ? row + NGW : row);
;         auto add_row = [&](const u32x2 (&y)[4]) {
; #pragma unroll
;             for (int j = 0; j < 4; ++j) { acc[j][0] += __uint_as_float(y[j].x << 16); acc[j][1] += __uint_as_float(y[j].x & 0xffff0000u); acc[j][2] += __uint_as_float(y[j].y << 16); acc[j][3] += __uint_as_float(y[j].y & 0xffff0000u); } };
;         if (!LAST && row >= ML) {
.LBB0_1176:
	v_readlane_b32 s0, v250, 28
	v_readlane_b32 s1, v250, 29
	s_nop 0
	v_add_u32_e32 v66, s0, v28
	v_cmp_gt_i32_e32 vcc, s20, v66
	v_cmp_lt_i32_e64 s[0:1], s21, v66
	s_nop 0
	v_cndmask_b32_e32 v46, v28, v66, vcc
	v_ashrrev_i32_e32 v47, 31, v46
	v_lshlrev_b64 v[30:31], 11, v[46:47]
	v_lshl_add_u64 v[36:37], v[6:7], 0, v[30:31]
	v_mul_u32_u24_e32 v47, 0x4200, v1
	v_add_u32_e32 v46, v46, v47
	global_load_dwordx2 v[30:31], v[36:37], off
	global_load_dwordx2 v[32:33], v[36:37], off offset:512
	global_load_dwordx2 v[34:35], v[36:37], off offset:1024
	s_nop 0
	global_load_dwordx2 v[36:37], v[36:37], off offset:1536
	v_ashrrev_i32_e32 v47, 31, v46
	v_lshl_add_u64 v[46:47], v[46:47], 2, s[6:7]
	global_load_dword v67, v[46:47], off
	v_cmp_gt_i32_e32 vcc, s22, v28
	s_and_saveexec_b64 s[16:17], vcc
	s_xor_b64 s[16:17], exec, s[16:17]
	s_cbranch_execz .LBB0_1184
	s_waitcnt vmcnt(5)
	v_cmp_lt_i32_e32 vcc, -1, v23
	s_and_b32 s12, vcc_lo, 0xffff
	s_cmp_eq_u32 s12, 0
	s_cbranch_scc1 .LBB0_1182
	v_mov_b32_e32 v46, 0
	v_mov_b32_e32 v47, v46
	v_mov_b32_e32 v48, v46
	v_mov_b32_e32 v49, v46
	v_mov_b32_e32 v50, v46
	v_mov_b32_e32 v51, v46
	v_mov_b32_e32 v52, v46
	v_mov_b32_e32 v53, v46
	v_mov_b32_e32 v54, v46
	v_mov_b32_e32 v55, v46
	v_mov_b32_e32 v56, v46
	v_mov_b32_e32 v57, v46
	v_mov_b32_e32 v58, v46
	v_mov_b32_e32 v59, v46
	v_mov_b32_e32 v60, v46
	v_mov_b32_e32 v61, v46
	s_branch .LBB0_1180

; template <int VPT>
; __device__ __forceinline__ void topk_list(const Params& p, LAS unsigned char* lds, const float* a, int N, int cap, int rowbase, int mbase, int e) {
;     ...
;     if (active) {
; #pragma unroll
;         for (int j = 0; j < VPT; ++j) {
;             const int i = tid * VPT + j, row = rowbase + i; int slot = -1;
;             if (k[j] > T) slot = gtb++;
;             else if (k[j] == T) { if (eqb < need) slot = G + eqb; ++eqb; }
;             if (slot >= 0) { const int m = mbase + slot; WSP(int, OFF_RIDX)[e * MEXP + m] = row; WSP(float, OFF_GATE)[e * MEXP + m] = __uint_as_float(k[j] >> 2); WSP(int, OFF_SLOT)[row * 16 + e] = m; }
;             else WSP(int, OFF_SLOT)[row * 16 + e] = -1;
;         }
.LBB0_2175:
	s_or_b64 exec, exec, s[52:53]
	s_mul_i32 s98, s92, 0x4200
	v_add_u32_e32 v28, s98, v8
	v_ashrrev_i32_e32 v29, 31, v28
	v_lshl_add_u64 v[28:29], v[28:29], 2, s[4:5]
	global_store_dword v[28:29], v5, off
	s_and_saveexec_b64 s[22:23], s[68:69]
	s_xor_b64 s[52:53], exec, s[22:23]
	v_cmp_lt_i32_e64 s[22:23], v2, v9
	v_sub_u32_e32 v4, v2, v9
	v_add_u32_e32 v4, 0x400, v4
	v_cndmask_b32_e64 v5, 0, 1, s[62:63]
	s_and_b64 s[22:23], s[62:63], s[22:23]
	v_add_u32_e32 v2, v2, v5
	v_cndmask_b32_e64 v5, -1, v4, s[22:23]
	s_or_saveexec_b64 s[22:23], s[52:53]
	v_mov_b32_e32 v4, v3
	s_xor_b64 exec, exec, s[22:23]
	v_add_u32_e32 v4, 1, v3
	v_mov_b32_e32 v5, v3
	s_or_b64 exec, exec, s[22:23]
	v_add3_u32 v8, s70, v6, 1
	v_mov_b32_e32 v3, -1
	v_cmp_lt_i32_e64 s[22:23], -1, v5
	s_and_saveexec_b64 s[52:53], s[22:23]
	s_cbranch_execz .LBB0_2181
	v_add_u32_e32 v3, s67, v5
	v_add_u32_e32 v28, s66, v3
	v_ashrrev_i32_e32 v29, 31, v28
	v_lshlrev_b64 v[28:29], 2, v[28:29]
	v_lshl_add_u64 v[30:31], s[96:97], 0, v[28:29]
	v_lshl_add_u64 v[28:29], s[80:81], 0, v[28:29]
	v_lshrrev_b32_e32 v5, 2, v27
	global_store_dword v[28:29], v8, off
	global_store_dword v[30:31], v5, off
.LBB0_2181:
	s_or_b64 exec, exec, s[52:53]
	s_mul_i32 s98, s92, 0x4200
	v_add_u32_e32 v28, s98, v8
	v_ashrrev_i32_e32 v29, 31, v28
	v_lshl_add_u64 v[28:29], v[28:29], 2, s[4:5]
	global_store_dword v[28:29], v3, off
	s_and_saveexec_b64 s[22:23], s[64:65]
	s_xor_b64 s[52:53], exec, s[22:23]
	v_cmp_lt_i32_e64 s[22:23], v2, v9
	v_sub_u32_e32 v3, v2, v9
	v_add_u32_e32 v3, 0x400, v3
	v_cndmask_b32_e64 v5, 0, 1, s[58:59]
	s_and_b64 s[22:23], s[58:59], s[22:23]
	v_add_u32_e32 v2, v2, v5
	v_cndmask_b32_e64 v5, -1, v3, s[22:23]
	s_or_saveexec_b64 s[22:23], s[52:53]
	v_mov_b32_e32 v3, v4
	s_xor_b64 exec, exec, s[22:23]
	v_add_u32_e32 v3, 1, v4
	v_mov_b32_e32 v5, v4
	s_or_b64 exec, exec, s[22:23]
	v_add3_u32 v8, s70, v6, 2
	v_mov_b32_e32 v4, -1
	v_cmp_lt_i32_e64 s[22:23], -1, v5
	s_and_saveexec_b64 s[52:53], s[22:23]
	s_cbranch_execz .LBB0_2187
	v_add_u32_e32 v4, s67, v5
	v_add_u32_e32 v28, s66, v4
	v_ashrrev_i32_e32 v29, 31, v28
	v_lshlrev_b64 v[28:29], 2, v[28:29]
	v_lshrrev_b32_e32 v5, 2, v26
	v_lshl_add_u64 v[26:27], s[80:81], 0, v[28:29]
	v_lshl_add_u64 v[30:31], s[96:97], 0, v[28:29]
	global_store_dword v[26:27], v8, off
	global_store_dword v[30:31], v5, off
.LBB0_2187:
	s_or_b64 exec, exec, s[52:53]
	s_mul_i32 s98, s92, 0x4200
	v_add_u32_e32 v26, s98, v8
	v_ashrrev_i32_e32 v27, 31, v26
	v_lshl_add_u64 v[26:27], v[26:27], 2, s[4:5]
	global_store_dword v[26:27], v4, off
	s_and_saveexec_b64 s[22:23], s[60:61]
	s_xor_b64 s[52:53], exec, s[22:23]
	v_cmp_lt_i32_e64 s[22:23], v2, v9
	v_sub_u32_e32 v4, v2, v9
	v_add_u32_e32 v4, 0x400, v4
	v_cndmask_b32_e64 v5, 0, 1, s[54:55]
	s_and_b64 s[22:23], s[54:55], s[22:23]
	v_add_u32_e32 v2, v2, v5
	v_cndmask_b32_e64 v5, -1, v4, s[22:23]
	s_or_saveexec_b64 s[22:23], s[52:53]
	v_mov_b32_e32 v4, v3
	s_xor_b64 exec, exec, s[22:23]
	v_add_u32_e32 v4, 1, v3
	v_mov_b32_e32 v5, v3
	s_or_b64 exec, exec, s[22:23]
	v_add3_u32 v8, s70, v6, 3
	v_mov_b32_e32 v3, -1
	v_cmp_lt_i32_e64 s[22:23], -1, v5
	s_and_saveexec_b64 s[52:53], s[22:23]
	s_cbranch_execz .LBB0_2193
	v_add_u32_e32 v3, s67, v5
	v_add_u32_e32 v26, s66, v3
	v_ashrrev_i32_e32 v27, 31, v26
	v_lshlrev_b64 v[26:27], 2, v[26:27]
	v_lshl_add_u64 v[28:29], s[96:97], 0, v[26:27]
	v_lshl_add_u64 v[26:27], s[80:81], 0, v[26:27]
	v_lshrrev_b32_e32 v5, 2, v25
	global_store_dword v[26:27], v8, off
	global_store_dword v[28:29], v5, off
.LBB0_2193:
	s_or_b64 exec, exec, s[52:53]
	s_mul_i32 s98, s92, 0x4200
	v_add_u32_e32 v26, s98, v8
	v_ashrrev_i32_e32 v27, 31, v26
	v_lshl_add_u64 v[26:27], v[26:27], 2, s[4:5]
	global_store_dword v[26:27], v3, off
	s_and_saveexec_b64 s[22:23], s[56:57]
	s_xor_b64 s[52:53], exec, s[22:23]
	v_cmp_lt_i32_e64 s[22:23], v2, v9
	v_sub_u32_e32 v3, v2, v9
	v_add_u32_e32 v3, 0x400, v3
	v_cndmask_b32_e64 v5, 0, 1, s[46:47]
	s_and_b64 s[22:23], s[46:47], s[22:23]
	v_add_u32_e32 v2, v2, v5
	v_cndmask_b32_e64 v5, -1, v3, s[22:23]
	s_or_saveexec_b64 s[22:23], s[52:53]
	v_mov_b32_e32 v3, v4
	s_xor_b64 exec, exec, s[22:23]
	v_add_u32_e32 v3, 1, v4
	v_mov_b32_e32 v5, v4
	s_or_b64 exec, exec, s[22:23]
	v_add3_u32 v8, s70, v6, 4
	v_mov_b32_e32 v4, -1
	v_cmp_lt_i32_e64 s[22:23], -1, v5
	s_and_saveexec_b64 s[46:47], s[22:23]
	s_cbranch_execz .LBB0_2199
	v_add_u32_e32 v4, s67, v5
	v_add_u32_e32 v26, s66, v4
	v_ashrrev_i32_e32 v27, 31, v26
	v_lshlrev_b64 v[26:27], 2, v[26:27]
	v_lshrrev_b32_e32 v5, 2, v24
	v_lshl_add_u64 v[24:25], s[80:81], 0, v[26:27]
	v_lshl_add_u64 v[28:29], s[96:97], 0, v[26:27]
	global_store_dword v[24:25], v8, off
	global_store_dword v[28:29], v5, off
.LBB0_2199:
	s_or_b64 exec, exec, s[46:47]
	s_mul_i32 s98, s92, 0x4200
	v_add_u32_e32 v24, s98, v8
	v_ashrrev_i32_e32 v25, 31, v24
	v_lshl_add_u64 v[24:25], v[24:25], 2, s[4:5]
	global_store_dword v[24:25], v4, off
	s_and_saveexec_b64 s[22:23], s[50:51]
	s_xor_b64 s[46:47], exec, s[22:23]
	v_cmp_lt_i32_e64 s[22:23], v2, v9
	v_sub_u32_e32 v4, v2, v9
	v_add_u32_e32 v4, 0x400, v4
	v_cndmask_b32_e64 v5, 0, 1, s[42:43]
	s_and_b64 s[22:23], s[42:43], s[22:23]
	v_add_u32_e32 v2, v2, v5
	v_cndmask_b32_e64 v5, -1, v4, s[22:23]
	s_or_saveexec_b64 s[22:23], s[46:47]
	v_mov_b32_e32 v4, v3
	s_xor_b64 exec, exec, s[22:23]
	v_add_u32_e32 v4, 1, v3
	v_mov_b32_e32 v5, v3
	s_or_b64 exec, exec, s[22:23]
	v_add3_u32 v8, s70, v6, 5
	v_mov_b32_e32 v3, -1
	v_cmp_lt_i32_e64 s[22:23], -1, v5
	s_and_saveexec_b64 s[42:43], s[22:23]
	s_cbranch_execz .LBB0_2205
	v_add_u32_e32 v3, s67, v5
	v_add_u32_e32 v24, s66, v3
	v_ashrrev_i32_e32 v25, 31, v24
	v_lshlrev_b64 v[24:25], 2, v[24:25]
	v_lshl_add_u64 v[26:27], s[96:97], 0, v[24:25]
	v_lshl_add_u64 v[24:25], s[80:81], 0, v[24:25]
	v_lshrrev_b32_e32 v5, 2, v23
	global_store_dword v[24:25], v8, off
	global_store_dword v[26:27], v5, off
; template <int VPT>
; __device__ __forceinline__ void topk_list(const Params& p, LAS unsigned char* lds, const float* a, int N, int cap, int rowbase, int mbase, int e) {
;     ...
;     if (active) {
; #pragma unroll
;         for (int j = 0; j < VPT; ++j) {
;             const int i = tid * VPT + j, row = rowbase + i; int slot = -1;
;             if (k[j] > T) slot = gtb++;
;             else if (k[j] == T) { if (eqb < need) slot = G + eqb; ++eqb; }
;             if (slot >= 0) { const int m = mbase + slot; WSP(int, OFF_RIDX)[e * MEXP + m] = row; WSP(float, OFF_GATE)[e * MEXP + m] = __uint_as_float(k[j] >> 2); WSP(int, OFF_SLOT)[row * 16 + e] = m; }
;             else WSP(int, OFF_SLOT)[row * 16 + e] = -1;
;         }
.LBB0_2205:
	s_or_b64 exec, exec, s[42:43]
	s_mul_i32 s98, s92, 0x4200
	v_add_u32_e32 v24, s98, v8
	v_ashrrev_i32_e32 v25, 31, v24
	v_lshl_add_u64 v[24:25], v[24:25], 2, s[4:5]
	global_store_dword v[24:25], v3, off
	s_and_saveexec_b64 s[22:23], s[44:45]
	s_xor_b64 s[42:43], exec, s[22:23]
	v_cmp_lt_i32_e64 s[22:23], v2, v9
	v_sub_u32_e32 v3, v2, v9
	v_add_u32_e32 v3, 0x400, v3
	v_cndmask_b32_e64 v5, 0, 1, s[38:39]
	s_and_b64 s[22:23], s[38:39], s[22:23]
	v_add_u32_e32 v2, v2, v5
	v_cndmask_b32_e64 v5, -1, v3, s[22:23]
	s_or_saveexec_b64 s[22:23], s[42:43]
	v_mov_b32_e32 v3, v4
	s_xor_b64 exec, exec, s[22:23]
	v_add_u32_e32 v3, 1, v4
	v_mov_b32_e32 v5, v4
	s_or_b64 exec, exec, s[22:23]
	v_add3_u32 v8, s70, v6, 6
	v_mov_b32_e32 v4, -1
	v_cmp_lt_i32_e64 s[22:23], -1, v5
	s_and_saveexec_b64 s[38:39], s[22:23]
	s_cbranch_execz .LBB0_2211
	v_add_u32_e32 v4, s67, v5
	v_add_u32_e32 v24, s66, v4
	v_ashrrev_i32_e32 v25, 31, v24
	v_lshlrev_b64 v[24:25], 2, v[24:25]
	v_lshrrev_b32_e32 v5, 2, v22
	v_lshl_add_u64 v[22:23], s[80:81], 0, v[24:25]
	v_lshl_add_u64 v[26:27], s[96:97], 0, v[24:25]
	global_store_dword v[22:23], v8, off
	global_store_dword v[26:27], v5, off
.LBB0_2211:
	s_or_b64 exec, exec, s[38:39]
	s_mul_i32 s98, s92, 0x4200
	v_add_u32_e32 v22, s98, v8
	v_ashrrev_i32_e32 v23, 31, v22
	v_lshl_add_u64 v[22:23], v[22:23], 2, s[4:5]
	global_store_dword v[22:23], v4, off
	s_and_saveexec_b64 s[22:23], s[40:41]
	s_xor_b64 s[38:39], exec, s[22:23]
	v_cmp_lt_i32_e64 s[22:23], v2, v9
	v_sub_u32_e32 v4, v2, v9
	v_add_u32_e32 v4, 0x400, v4
	v_cndmask_b32_e64 v5, 0, 1, s[34:35]
	s_and_b64 s[22:23], s[34:35], s[22:23]
	v_add_u32_e32 v2, v2, v5
	v_cndmask_b32_e64 v5, -1, v4, s[22:23]
	s_or_saveexec_b64 s[22:23], s[38:39]
	v_mov_b32_e32 v4, v3
	s_xor_b64 exec, exec, s[22:23]
	v_add_u32_e32 v4, 1, v3
	v_mov_b32_e32 v5, v3
	s_or_b64 exec, exec, s[22:23]
	v_add3_u32 v8, s70, v6, 7
	v_mov_b32_e32 v3, -1
	v_cmp_lt_i32_e64 s[22:23], -1, v5
	s_and_saveexec_b64 s[34:35], s[22:23]
	s_cbranch_execz .LBB0_2217
	v_add_u32_e32 v3, s67, v5
	v_add_u32_e32 v22, s66, v3
	v_ashrrev_i32_e32 v23, 31, v22
	v_lshlrev_b64 v[22:23], 2, v[22:23]
	v_lshl_add_u64 v[24:25], s[96:97], 0, v[22:23]
	v_lshl_add_u64 v[22:23], s[80:81], 0, v[22:23]
	v_lshrrev_b32_e32 v5, 2, v21
	global_store_dword v[22:23], v8, off
	global_store_dword v[24:25], v5, off
.LBB0_2217:
	s_or_b64 exec, exec, s[34:35]
	s_mul_i32 s98, s92, 0x4200
	v_add_u32_e32 v22, s98, v8
	v_ashrrev_i32_e32 v23, 31, v22
	v_lshl_add_u64 v[22:23], v[22:23], 2, s[4:5]
	global_store_dword v[22:23], v3, off
	s_and_saveexec_b64 s[22:23], s[36:37]
	s_xor_b64 s[34:35], exec, s[22:23]
	v_cmp_lt_i32_e64 s[22:23], v2, v9
	v_sub_u32_e32 v3, v2, v9
	v_add_u32_e32 v3, 0x400, v3
	v_cndmask_b32_e64 v5, 0, 1, s[28:29]
	s_and_b64 s[22:23], s[28:29], s[22:23]
	v_add_u32_e32 v2, v2, v5
	v_cndmask_b32_e64 v5, -1, v3, s[22:23]
	s_or_saveexec_b64 s[22:23], s[34:35]
	v_mov_b32_e32 v3, v4
	s_xor_b64 exec, exec, s[22:23]
	v_add_u32_e32 v3, 1, v4
	v_mov_b32_e32 v5, v4
	s_or_b64 exec, exec, s[22:23]
	v_add3_u32 v8, s70, v6, 8
	v_mov_b32_e32 v4, -1
	v_cmp_lt_i32_e64 s[22:23], -1, v5
	s_and_saveexec_b64 s[28:29], s[22:23]
	s_cbranch_execz .LBB0_2223
	v_add_u32_e32 v4, s67, v5
	v_add_u32_e32 v22, s66, v4
	v_ashrrev_i32_e32 v23, 31, v22
	v_lshlrev_b64 v[22:23], 2, v[22:23]
	v_lshrrev_b32_e32 v5, 2, v20
	v_lshl_add_u64 v[20:21], s[80:81], 0, v[22:23]
	v_lshl_add_u64 v[24:25], s[96:97], 0, v[22:23]
	global_store_dword v[20:21], v8, off
	global_store_dword v[24:25], v5, off
.LBB0_2223:
	s_or_b64 exec, exec, s[28:29]
	s_mul_i32 s98, s92, 0x4200
	v_add_u32_e32 v20, s98, v8
	v_ashrrev_i32_e32 v21, 31, v20
	v_lshl_add_u64 v[20:21], v[20:21], 2, s[4:5]
	global_store_dword v[20:21], v4, off
	s_and_saveexec_b64 s[22:23], s[30:31]
	s_xor_b64 s[28:29], exec, s[22:23]
	v_cmp_lt_i32_e64 s[22:23], v2, v9
	v_sub_u32_e32 v4, v2, v9
	v_add_u32_e32 v4, 0x400, v4
	v_cndmask_b32_e64 v5, 0, 1, s[24:25]
	s_and_b64 s[22:23], s[24:25], s[22:23]
	v_add_u32_e32 v2, v2, v5
	v_cndmask_b32_e64 v5, -1, v4, s[22:23]
	s_or_saveexec_b64 s[22:23], s[28:29]
	v_mov_b32_e32 v4, v3
	s_xor_b64 exec, exec, s[22:23]
	v_add_u32_e32 v4, 1, v3
	v_mov_b32_e32 v5, v3
	s_or_b64 exec, exec, s[22:23]
	v_add3_u32 v8, s70, v6, 9
	v_mov_b32_e32 v3, -1
	v_cmp_lt_i32_e64 s[22:23], -1, v5
	s_and_saveexec_b64 s[24:25], s[22:23]
	s_cbranch_execz .LBB0_2229
	v_add_u32_e32 v3, s67, v5
	v_add_u32_e32 v20, s66, v3
	v_ashrrev_i32_e32 v21, 31, v20
	v_lshlrev_b64 v[20:21], 2, v[20:21]
	v_lshl_add_u64 v[22:23], s[96:97], 0, v[20:21]
	v_lshl_add_u64 v[20:21], s[80:81], 0, v[20:21]
	v_lshrrev_b32_e32 v5, 2, v19
	global_store_dword v[20:21], v8, off
	global_store_dword v[22:23], v5, off
.LBB0_2229:
	s_or_b64 exec, exec, s[24:25]
	s_mul_i32 s98, s92, 0x4200
	v_add_u32_e32 v20, s98, v8
	v_ashrrev_i32_e32 v21, 31, v20
	v_lshl_add_u64 v[20:21], v[20:21], 2, s[4:5]
	global_store_dword v[20:21], v3, off
	s_and_saveexec_b64 s[22:23], s[26:27]
	s_xor_b64 s[24:25], exec, s[22:23]
	v_cmp_lt_i32_e64 s[22:23], v2, v9
	v_sub_u32_e32 v3, v2, v9
	v_add_u32_e32 v3, 0x400, v3
	v_cndmask_b32_e64 v5, 0, 1, s[18:19]
	s_and_b64 s[18:19], s[18:19], s[22:23]
	v_add_u32_e32 v2, v2, v5
	v_cndmask_b32_e64 v5, -1, v3, s[18:19]
	s_or_saveexec_b64 s[18:19], s[24:25]
	v_mov_b32_e32 v3, v4
	s_xor_b64 exec, exec, s[18:19]
	v_add_u32_e32 v3, 1, v4
	v_mov_b32_e32 v5, v4
	s_or_b64 exec, exec, s[18:19]
	v_add3_u32 v8, s70, v6, 10
	v_mov_b32_e32 v4, -1
	v_cmp_lt_i32_e64 s[18:19], -1, v5
	s_and_saveexec_b64 s[22:23], s[18:19]
	s_cbranch_execz .LBB0_2235
	v_add_u32_e32 v4, s67, v5
	v_add_u32_e32 v20, s66, v4
	v_ashrrev_i32_e32 v21, 31, v20
	v_lshlrev_b64 v[20:21], 2, v[20:21]
	v_lshrrev_b32_e32 v5, 2, v18
	v_lshl_add_u64 v[18:19], s[80:81], 0, v[20:21]
	v_lshl_add_u64 v[22:23], s[96:97], 0, v[20:21]
	global_store_dword v[18:19], v8, off
	global_store_dword v[22:23], v5, off
; template <int VPT>
; __device__ __forceinline__ void topk_list(const Params& p, LAS unsigned char* lds, const float* a, int N, int cap, int rowbase, int mbase, int e) {
;     ...
;     if (active) {
; #pragma unroll
;         for (int j = 0; j < VPT; ++j) {
;             const int i = tid * VPT + j, row = rowbase + i; int slot = -1;
;             if (k[j] > T) slot = gtb++;
;             else if (k[j] == T) { if (eqb < need) slot = G + eqb; ++eqb; }
;             if (slot >= 0) { const int m = mbase + slot; WSP(int, OFF_RIDX)[e * MEXP + m] = row; WSP(float, OFF_GATE)[e * MEXP + m] = __uint_as_float(k[j] >> 2); WSP(int, OFF_SLOT)[row * 16 + e] = m; }
;             else WSP(int, OFF_SLOT)[row * 16 + e] = -1;
;         }
.LBB0_2235:
	s_or_b64 exec, exec, s[22:23]
	s_mul_i32 s98, s92, 0x4200
	v_add_u32_e32 v18, s98, v8
	v_ashrrev_i32_e32 v19, 31, v18
	v_lshl_add_u64 v[18:19], v[18:19], 2, s[4:5]
	global_store_dword v[18:19], v4, off
	s_and_saveexec_b64 s[18:19], s[20:21]
	s_xor_b64 s[20:21], exec, s[18:19]
	v_cmp_lt_i32_e64 s[18:19], v2, v9
	v_sub_u32_e32 v4, v2, v9
	v_add_u32_e32 v4, 0x400, v4
	v_cndmask_b32_e64 v5, 0, 1, s[14:15]
	s_and_b64 s[14:15], s[14:15], s[18:19]
	v_add_u32_e32 v2, v2, v5
	v_cndmask_b32_e64 v5, -1, v4, s[14:15]
	s_or_saveexec_b64 s[14:15], s[20:21]
	v_mov_b32_e32 v4, v3
	s_xor_b64 exec, exec, s[14:15]
	v_add_u32_e32 v4, 1, v3
	v_mov_b32_e32 v5, v3
	s_or_b64 exec, exec, s[14:15]
	v_add3_u32 v8, s70, v6, 11
	v_mov_b32_e32 v3, -1
	v_cmp_lt_i32_e64 s[14:15], -1, v5
	s_and_saveexec_b64 s[18:19], s[14:15]
	s_cbranch_execz .LBB0_2241
	v_add_u32_e32 v3, s67, v5
	v_add_u32_e32 v18, s66, v3
	v_ashrrev_i32_e32 v19, 31, v18
	v_lshlrev_b64 v[18:19], 2, v[18:19]
	v_lshl_add_u64 v[20:21], s[96:97], 0, v[18:19]
	v_lshl_add_u64 v[18:19], s[80:81], 0, v[18:19]
	v_lshrrev_b32_e32 v5, 2, v17
	global_store_dword v[18:19], v8, off
	global_store_dword v[20:21], v5, off
.LBB0_2241:
	s_or_b64 exec, exec, s[18:19]
	s_mul_i32 s98, s92, 0x4200
	v_add_u32_e32 v18, s98, v8
	v_ashrrev_i32_e32 v19, 31, v18
	v_lshl_add_u64 v[18:19], v[18:19], 2, s[4:5]
	global_store_dword v[18:19], v3, off
	s_and_saveexec_b64 s[14:15], s[16:17]
	s_xor_b64 s[16:17], exec, s[14:15]
	v_cmp_lt_i32_e64 s[14:15], v2, v9
	v_sub_u32_e32 v3, v2, v9
	v_add_u32_e32 v3, 0x400, v3
	v_cndmask_b32_e64 v5, 0, 1, s[10:11]
	s_and_b64 s[10:11], s[10:11], s[14:15]
	v_add_u32_e32 v2, v2, v5
	v_cndmask_b32_e64 v5, -1, v3, s[10:11]
	s_or_saveexec_b64 s[10:11], s[16:17]
	v_mov_b32_e32 v3, v4
	s_xor_b64 exec, exec, s[10:11]
	v_add_u32_e32 v3, 1, v4
	v_mov_b32_e32 v5, v4
	s_or_b64 exec, exec, s[10:11]
	v_add3_u32 v8, s70, v6, 12
	v_mov_b32_e32 v4, -1
	v_cmp_lt_i32_e64 s[10:11], -1, v5
	s_and_saveexec_b64 s[14:15], s[10:11]
	s_cbranch_execz .LBB0_2247
	v_add_u32_e32 v4, s67, v5
	v_add_u32_e32 v18, s66, v4
	v_ashrrev_i32_e32 v19, 31, v18
	v_lshlrev_b64 v[18:19], 2, v[18:19]
	v_lshrrev_b32_e32 v5, 2, v16
	v_lshl_add_u64 v[16:17], s[80:81], 0, v[18:19]
	v_lshl_add_u64 v[20:21], s[96:97], 0, v[18:19]
	global_store_dword v[16:17], v8, off
	global_store_dword v[20:21], v5, off
.LBB0_2247:
	s_or_b64 exec, exec, s[14:15]
	s_mul_i32 s98, s92, 0x4200
	v_add_u32_e32 v16, s98, v8
	v_ashrrev_i32_e32 v17, 31, v16
	v_lshl_add_u64 v[16:17], v[16:17], 2, s[4:5]
	global_store_dword v[16:17], v4, off
	s_and_saveexec_b64 s[10:11], s[12:13]
	s_xor_b64 s[12:13], exec, s[10:11]
	v_cmp_lt_i32_e64 s[10:11], v2, v9
	v_sub_u32_e32 v4, v2, v9
	v_add_u32_e32 v4, 0x400, v4
	v_cndmask_b32_e64 v5, 0, 1, s[6:7]
	s_and_b64 s[6:7], s[6:7], s[10:11]
	v_add_u32_e32 v2, v2, v5
	v_cndmask_b32_e64 v5, -1, v4, s[6:7]
	s_or_saveexec_b64 s[6:7], s[12:13]
	v_mov_b32_e32 v4, v3
	s_xor_b64 exec, exec, s[6:7]
	v_add_u32_e32 v4, 1, v3
	v_mov_b32_e32 v5, v3
	s_or_b64 exec, exec, s[6:7]
	v_add3_u32 v8, s70, v6, 13
	v_mov_b32_e32 v3, -1
	v_cmp_lt_i32_e64 s[6:7], -1, v5
	s_and_saveexec_b64 s[10:11], s[6:7]
	s_cbranch_execz .LBB0_2253
	v_add_u32_e32 v3, s67, v5
	v_add_u32_e32 v16, s66, v3
	v_ashrrev_i32_e32 v17, 31, v16
	v_lshlrev_b64 v[16:17], 2, v[16:17]
	v_lshl_add_u64 v[18:19], s[96:97], 0, v[16:17]
	v_lshl_add_u64 v[16:17], s[80:81], 0, v[16:17]
	v_lshrrev_b32_e32 v5, 2, v15
	global_store_dword v[16:17], v8, off
	global_store_dword v[18:19], v5, off
.LBB0_2253:
	s_or_b64 exec, exec, s[10:11]
	s_mul_i32 s98, s92, 0x4200
	v_add_u32_e32 v16, s98, v8
	v_ashrrev_i32_e32 v17, 31, v16
	v_lshl_add_u64 v[16:17], v[16:17], 2, s[4:5]
	global_store_dword v[16:17], v3, off
	s_and_saveexec_b64 s[6:7], s[8:9]
	s_xor_b64 s[8:9], exec, s[6:7]
	v_cmp_lt_i32_e64 s[6:7], v2, v9
	v_sub_u32_e32 v3, v2, v9
	v_add_u32_e32 v3, 0x400, v3
	v_cndmask_b32_e64 v5, 0, 1, s[2:3]
	s_and_b64 s[2:3], s[2:3], s[6:7]
	v_add_u32_e32 v2, v2, v5
	v_cndmask_b32_e64 v8, -1, v3, s[2:3]
	s_or_saveexec_b64 s[2:3], s[8:9]
	v_mov_b32_e32 v5, v4
	s_xor_b64 exec, exec, s[2:3]
	v_add_u32_e32 v5, 1, v4
	v_mov_b32_e32 v8, v4
	s_or_b64 exec, exec, s[2:3]
	v_add3_u32 v15, s70, v6, 14
	v_mov_b32_e32 v3, -1
	v_cmp_lt_i32_e64 s[2:3], -1, v8
	v_mov_b32_e32 v4, -1
	s_and_saveexec_b64 s[6:7], s[2:3]
	s_cbranch_execz .LBB0_2259
	v_add_u32_e32 v4, s67, v8
	v_add_u32_e32 v16, s66, v4
	v_ashrrev_i32_e32 v17, 31, v16
	v_lshlrev_b64 v[16:17], 2, v[16:17]
	v_lshl_add_u64 v[18:19], s[96:97], 0, v[16:17]
	v_lshl_add_u64 v[16:17], s[80:81], 0, v[16:17]
	v_lshrrev_b32_e32 v8, 2, v14
	global_store_dword v[16:17], v15, off
	global_store_dword v[18:19], v8, off
.LBB0_2259:
	s_or_b64 exec, exec, s[6:7]
	v_cmp_lt_i32_e64 s[2:3], v2, v9
	v_sub_u32_e32 v2, v2, v9
	s_mul_i32 s98, s92, 0x4200
	v_add_u32_e32 v14, s98, v15
	v_add_u32_e32 v2, 0x400, v2
	s_and_b64 s[0:1], s[0:1], s[2:3]
	v_ashrrev_i32_e32 v15, 31, v14
	v_cndmask_b32_e64 v2, -1, v2, s[0:1]
	v_lshl_add_u64 v[14:15], v[14:15], 2, s[4:5]
	v_cndmask_b32_e32 v2, v2, v5, vcc
	global_store_dword v[14:15], v4, off
	v_add3_u32 v4, s70, v6, 15
	v_cmp_lt_i32_e32 vcc, -1, v2
	s_and_saveexec_b64 s[0:1], vcc
	s_cbranch_execz .LBB0_2261
	v_add_u32_e32 v3, s67, v2
	v_add_u32_e32 v8, s66, v3
	v_ashrrev_i32_e32 v9, 31, v8
	v_lshlrev_b64 v[8:9], 2, v[8:9]
	v_lshrrev_b32_e32 v2, 2, v7
	v_lshl_add_u64 v[6:7], s[80:81], 0, v[8:9]
	v_lshl_add_u64 v[14:15], s[96:97], 0, v[8:9]
	global_store_dword v[6:7], v4, off
	global_store_dword v[14:15], v2, off
.LBB0_2261:
	s_or_b64 exec, exec, s[0:1]
	s_mul_i32 s98, s92, 0x4200
	v_add_u32_e32 v4, s98, v4
	v_ashrrev_i32_e32 v5, 31, v4
	v_lshl_add_u64 v[4:5], v[4:5], 2, s[4:5]
	global_store_dword v[4:5], v3, off

; template <bool LAST>
; __device__ __forceinline__ void ph_combine(const int vc, const Params& p, int layer, int rows) {
;     ...
;     u32x2 xn[4]; int son = -1;
;     auto prefetch = [&](int row) { const bf16_t* xr = WSP(bf16_t, OFF_X) + (size_t)row * D;
; #pragma unroll
;         for (int j = 0; j < 4; ++j) xn[j] = ((const u32x2*)xr)[lane + 64 * j];
;         son = WSP(int, OFF_SLOT)[row * 16 + (lane & 15)]; };
;     if (gw < rows) prefetch(gw);
;     for (int row = gw; row < rows; row += NGW) {
;         f32x4 v[4], acc[4];
; #pragma unroll
;         for (int j = 0; j < 4; ++j) { v[j] = (f32x4){__uint_as_float(xn[j].x << 16), __uint_as_float(xn[j].x & 0xffff0000u), __uint_as_float(xn[j].y << 16), __uint_as_float(xn[j].y & 0xffff0000u)}; acc[j] = (f32x4){0.f, 0.f, 0.f, 0.f}; }
;         const int so = son;
;         prefetch(row + NGW < rows ? row + NGW : row);
.LBB0_2470:
	s_or_b64 exec, exec, s[0:1]
	s_waitcnt lgkmcnt(0)
	s_barrier
	s_movk_i32 s8, 0x4000
	v_ashrrev_i32_e32 v1, 6, v0
	v_add_u32_e32 v10, v1, v198
	v_cmp_gt_i32_e32 vcc, s8, v10
	s_and_saveexec_b64 s[0:1], vcc
	s_cbranch_execz .LBB0_2478
	s_add_u32 s0, s90, 0x13600
	v_ashrrev_i32_e32 v11, 31, v10
	v_and_b32_e32 v12, 63, v0
	s_addc_u32 s1, s91, 0
	v_lshlrev_b64 v[2:3], 11, v[10:11]
	v_lshl_add_u64 v[4:5], s[0:1], 0, v[2:3]
	v_mov_b32_e32 v3, 0
	v_lshlrev_b32_e32 v2, 3, v12
	v_and_b32_e32 v50, 15, v0
	v_lshl_add_u64 v[4:5], v[4:5], 0, v[2:3]
	s_add_u32 s2, s90, 0x51b87600
	v_mul_u32_u24_e32 v0, 0x4200, v50
	v_add_u32_e32 v0, v0, v10
	global_load_dwordx2 v[32:33], v[4:5], off
	global_load_dwordx2 v[30:31], v[4:5], off offset:512
	global_load_dwordx2 v[28:29], v[4:5], off offset:1024
	global_load_dwordx2 v[26:27], v[4:5], off offset:1536
	s_addc_u32 s3, s91, 0
	v_ashrrev_i32_e32 v1, 31, v0
	v_lshl_add_u64 v[0:1], v[0:1], 2, s[2:3]
	global_load_dword v11, v[0:1], off
	v_or_b32_e32 v14, 64, v12
	v_or_b32_e32 v16, 0x80, v12
	v_or_b32_e32 v18, 0xc0, v12
	v_lshlrev_b32_e32 v6, 4, v12
	v_mov_b32_e32 v7, v3
	v_lshl_add_u64 v[0:1], s[0:1], 0, v[2:3]
	v_lshl_add_u64 v[4:5], s[86:87], 0, v[6:7]
	v_lshl_add_u64 v[6:7], s[88:89], 0, v[6:7]
	v_lshl_add_u64 v[8:9], s[84:85], 0, v[2:3]
	s_mov_b64 s[4:5], 0
	s_movk_i32 s9, 0x3fff
	s_mov_b64 s[6:7], 0x51a2a600
	v_lshlrev_b32_e32 v2, 4, v12
	v_lshlrev_b32_e32 v12, 4, v14
	v_lshlrev_b32_e32 v14, 4, v16
	v_lshlrev_b32_e32 v16, 4, v18
	v_mov_b32_e32 v51, 0x358637bd
	s_mov_b32 s10, 0x800000
	s_branch .LBB0_2473

; template <bool LAST>
; __device__ __forceinline__ void ph_combine(const int vc, const Params& p, int layer, int rows) {
;     ...
;     for (int row = gw; row < rows; row += NGW) {
;         f32x4 v[4], acc[4];
; #pragma unroll
;         for (int j = 0; j < 4; ++j) { v[j] = (f32x4){__uint_as_float(xn[j].x << 16), __uint_as_float(xn[j].x & 0xffff0000u), __uint_as_float(xn[j].y << 16), __uint_as_float(xn[j].y & 0xffff0000u)}; acc[j] = (f32x4){0.f, 0.f, 0.f, 0.f}; }
;         const int so = son;
;         prefetch(row + NGW < rows ? row + NGW : row);
;         auto add_row = [&](const u32x2 (&y)[4]) {
; #pragma unroll
;             for (int j = 0; j < 4; ++j) { acc[j][0] += __uint_as_float(y[j].x << 16); acc[j][1] += __uint_as_float(y[j].x & 0xffff0000u); acc[j][2] += __uint_as_float(y[j].y << 16); acc[j][3] += __uint_as_float(y[j].y & 0xffff0000u); } };
;         if (!LAST && row >= ML) {
; #pragma unroll 1
;             for (int e = 0; e < 16; ++e) { const int m = __builtin_amdgcn_readlane(so, e);
;                 if (m >= 0) { const bf16_t* yr = WSP(bf16_t, OFF_YEB) + ((size_t)e * MEXP + m) * D;
; #pragma unroll 1
;                     for (int pt = 0; pt < 4; ++pt, yr += (size_t)64 * D) { u32x2 y[4];
; #pragma unroll
;                         for (int j = 0; j < 4; ++j) y[j] = __builtin_nontemporal_load((const u32x2*)yr + lane + 64 * j);
;                         add_row(y); } } }
;         } else {
;             unsigned sel = (unsigned)__builtin_amdgcn_ballot_w64(so >= 0) & 0xffffu;
.LBB0_2473:
	v_add_u32_e32 v52, s60, v10
	v_cmp_gt_i32_e32 vcc, s8, v52
	v_cmp_lt_i32_e64 s[0:1], s9, v52
	v_mov_b32_e32 v49, 0
	v_cndmask_b32_e32 v34, v10, v52, vcc
	v_ashrrev_i32_e32 v35, 31, v34
	v_lshlrev_b64 v[18:19], 11, v[34:35]
	v_lshl_add_u64 v[36:37], v[0:1], 0, v[18:19]
	v_mul_u32_u24_e32 v35, 0x4200, v50
	v_add_u32_e32 v34, v34, v35
	global_load_dwordx2 v[18:19], v[36:37], off
	global_load_dwordx2 v[20:21], v[36:37], off offset:512
	global_load_dwordx2 v[22:23], v[36:37], off offset:1024
	global_load_dwordx2 v[24:25], v[36:37], off offset:1536
	v_ashrrev_i32_e32 v35, 31, v34
	v_lshl_add_u64 v[34:35], v[34:35], 2, s[2:3]
	global_load_dword v53, v[34:35], off
	s_waitcnt vmcnt(5)
	v_cmp_lt_i32_e32 vcc, -1, v11
	s_and_b32 s11, vcc_lo, 0xffff
	s_cmp_eq_u32 s11, 0
	v_mov_b32_e32 v48, 0
	v_mov_b32_e32 v47, 0
	v_mov_b32_e32 v46, 0
	v_mov_b32_e32 v45, 0
	v_mov_b32_e32 v44, 0
	v_mov_b32_e32 v43, 0
	v_mov_b32_e32 v42, 0
	v_mov_b32_e32 v41, 0
	v_mov_b32_e32 v40, 0
	v_mov_b32_e32 v39, 0
	v_mov_b32_e32 v38, 0
	v_mov_b32_e32 v37, 0
	v_mov_b32_e32 v36, 0
	v_mov_b32_e32 v35, 0
	v_mov_b32_e32 v34, 0
	s_cbranch_scc1 .LBB0_2472
	v_mov_b32_e32 v34, 0
	v_mov_b32_e32 v35, v34
	v_mov_b32_e32 v36, v34
	v_mov_b32_e32 v37, v34
	v_mov_b32_e32 v38, v34
	v_mov_b32_e32 v39, v34
	v_mov_b32_e32 v40, v34
	v_mov_b32_e32 v41, v34
	v_mov_b32_e32 v42, v34
	v_mov_b32_e32 v43, v34
	v_mov_b32_e32 v44, v34
	v_mov_b32_e32 v45, v34
	v_mov_b32_e32 v46, v34
	v_mov_b32_e32 v47, v34
	v_mov_b32_e32 v48, v34
	v_mov_b32_e32 v49, v34
	s_branch .LBB0_2476

; #define LAS __attribute__((address_space(3)))
; __device__ __forceinline__ unsigned xb_ld(unsigned* p)              { return __hip_atomic_load(p, __ATOMIC_RELAXED, __HIP_MEMORY_SCOPE_AGENT); }
; __device__ __forceinline__ unsigned xb_add(unsigned* p, unsigned v) { return __hip_atomic_fetch_add(p, v, __ATOMIC_RELAXED, __HIP_MEMORY_SCOPE_AGENT); }
; __device__ __forceinline__ unsigned xb_xcc_id() { return (unsigned)__builtin_amdgcn_s_getreg((3 << 11) | 20) & 0xFu; }
; __global__ __launch_bounds__(NTHR, 2) void mega(Params p) {
;     extern __shared__ __attribute__((aligned(16))) unsigned char smem[];
;     LAS unsigned char* lds = (LAS unsigned char*)smem;
;     volatile LAS unsigned* st = (volatile LAS unsigned*)(lds + LDS_BYTES - 16);
;     if (threadIdx.x == 0) { st[0] = 0u; st[1] = 0u; st[2] = 0u; st[3] = 0u; }
;     __syncthreads();
;     XcdBarrier bar; bar.bar = WSP(unsigned, OFF_BAR); bar.x = xb_xcc_id(); bar.st = st;
;     if (threadIdx.x == 0) st[2] = xb_add(&bar.bar[XB_XCNT(bar.x)], 1u);
;     run_phase<0>((int)blockIdx.x, p, lds);
;     xcd_barrier(bar);
;     if (threadIdx.x == 0) {
;         bool uni = gridDim.x == 256;
; #pragma unroll
;         for (unsigned j = 0; j < 16; ++j) { const unsigned cnt = xb_ld(&bar.bar[XB_XCNT(j)]); uni = uni && (cnt == (j < 8 ? 32u : 0u)); }
;         st[3] = uni ? st[2] * 8u + bar.x : blockIdx.x;
;     }
;     __syncthreads();
;     const int vc = (int)st[3];
;     run_all<1>(vc, p, lds, bar);
; }
	.amdhsa_kernel _ZN12_GLOBAL__N_14megaENS_6ParamsE
		.amdhsa_group_segment_fixed_size 0
		.amdhsa_private_segment_fixed_size 0
		.amdhsa_kernarg_size 448
		.amdhsa_user_sgpr_count 2
		.amdhsa_user_sgpr_dispatch_ptr 0
		.amdhsa_user_sgpr_queue_ptr 0
		.amdhsa_user_sgpr_kernarg_segment_ptr 1
		.amdhsa_user_sgpr_dispatch_id 0
		.amdhsa_user_sgpr_kernarg_preload_length 0
		.amdhsa_user_sgpr_kernarg_preload_offset 0
		.amdhsa_user_sgpr_private_segment_size 0
		.amdhsa_uses_dynamic_stack 0
		.amdhsa_enable_private_segment 0
		.amdhsa_system_sgpr_workgroup_id_x 1
		.amdhsa_system_sgpr_workgroup_id_y 0
		.amdhsa_system_sgpr_workgroup_id_z 0
		.amdhsa_system_sgpr_workgroup_info 0
		.amdhsa_system_vgpr_workitem_id 0
		.amdhsa_next_free_vgpr 251
		.amdhsa_next_free_sgpr 100
		.amdhsa_accum_offset 252
		.amdhsa_reserve_vcc 1
		.amdhsa_float_round_mode_32 0
		.amdhsa_float_round_mode_16_64 0
		.amdhsa_float_denorm_mode_32 3
		.amdhsa_float_denorm_mode_16_64 3
		.amdhsa_dx10_clamp 1
		.amdhsa_ieee_mode 1
		.amdhsa_fp16_overflow 0
		.amdhsa_tg_split 0
		.amdhsa_exception_fp_ieee_invalid_op 0
		.amdhsa_exception_fp_denorm_src 0
		.amdhsa_exception_fp_ieee_div_zero 0
		.amdhsa_exception_fp_ieee_overflow 0
		.amdhsa_exception_fp_ieee_underflow 0
		.amdhsa_exception_fp_ieee_inexact 0
		.amdhsa_exception_int_div_zero 0
	.end_amdhsa_kernel

; #define LAS __attribute__((address_space(3)))
; __device__ __forceinline__ unsigned xb_ld(unsigned* p)              { return __hip_atomic_load(p, __ATOMIC_RELAXED, __HIP_MEMORY_SCOPE_AGENT); }
; __device__ __forceinline__ unsigned xb_add(unsigned* p, unsigned v) { return __hip_atomic_fetch_add(p, v, __ATOMIC_RELAXED, __HIP_MEMORY_SCOPE_AGENT); }
; __device__ __forceinline__ unsigned xb_xcc_id() { return (unsigned)__builtin_amdgcn_s_getreg((3 << 11) | 20) & 0xFu; }
; __global__ __launch_bounds__(NTHR, 2) void mega(Params p) {
;     extern __shared__ __attribute__((aligned(16))) unsigned char smem[];
;     LAS unsigned char* lds = (LAS unsigned char*)smem;
;     volatile LAS unsigned* st = (volatile LAS unsigned*)(lds + LDS_BYTES - 16);
;     if (threadIdx.x == 0) { st[0] = 0u; st[1] = 0u; st[2] = 0u; st[3] = 0u; }
;     __syncthreads();
;     XcdBarrier bar; bar.bar = WSP(unsigned, OFF_BAR); bar.x = xb_xcc_id(); bar.st = st;
;     if (threadIdx.x == 0) st[2] = xb_add(&bar.bar[XB_XCNT(bar.x)], 1u);
;     run_phase<0>((int)blockIdx.x, p, lds);
;     xcd_barrier(bar);
;     if (threadIdx.x == 0) {
;         bool uni = gridDim.x == 256;
; #pragma unroll
;         for (unsigned j = 0; j < 16; ++j) { const unsigned cnt = xb_ld(&bar.bar[XB_XCNT(j)]); uni = uni && (cnt == (j < 8 ? 32u : 0u)); }
;         st[3] = uni ? st[2] * 8u + bar.x : blockIdx.x;
;     }
;     __syncthreads();
;     const int vc = (int)st[3];
;     run_all<1>(vc, p, lds, bar);
; }
amdhsa.kernels:
  - .agpr_count:     0
    .args:
      - .offset:         0
        .size:           192
        .value_kind:     by_value
      - .offset:         192
        .size:           4
        .value_kind:     hidden_block_count_x
      - .offset:         196
        .size:           4
        .value_kind:     hidden_block_count_y
      - .offset:         200
        .size:           4
        .value_kind:     hidden_block_count_z
      - .offset:         204
        .size:           2
        .value_kind:     hidden_group_size_x
      - .offset:         206
        .size:           2
        .value_kind:     hidden_group_size_y
      - .offset:         208
        .size:           2
        .value_kind:     hidden_group_size_z
      - .offset:         210
        .size:           2
        .value_kind:     hidden_remainder_x
      - .offset:         212
        .size:           2
        .value_kind:     hidden_remainder_y
      - .offset:         214
        .size:           2
        .value_kind:     hidden_remainder_z
      - .offset:         232
        .size:           8
        .value_kind:     hidden_global_offset_x
      - .offset:         240
        .size:           8
        .value_kind:     hidden_global_offset_y
      - .offset:         248
        .size:           8
        .value_kind:     hidden_global_offset_z
      - .offset:         256
        .size:           2
        .value_kind:     hidden_grid_dims
      - .offset:         312
        .size:           4
        .value_kind:     hidden_dynamic_lds_size
    .group_segment_fixed_size: 0
    .kernarg_segment_align: 8
    .kernarg_segment_size: 448
    .language:       OpenCL C
    .language_version:
      - 2
      - 0
    .max_flat_workgroup_size: 512
    .name:           _ZN12_GLOBAL__N_14megaENS_6ParamsE
    .private_segment_fixed_size: 0
    .sgpr_count:     106
    .sgpr_spill_count: 59
    .symbol:         _ZN12_GLOBAL__N_14megaENS_6ParamsE.kd
    .uniform_work_group_size: 1
    .uses_dynamic_stack: false
    .vgpr_count:     251
    .vgpr_spill_count: 0
    .wavefront_size: 64
